# nca kernels: per-row window/image masks of the QK accumulator init precomputed as 7 SGPR-pair masks in the load-wait shadow before barrier 1; 42 VALU per wave removed from the QK phase
# speedup vs baseline: 1.0121x; 1.0121x over previous
.LBB1_14:
	s_or_b64 exec, exec, s[14:15]
	s_movk_i32 s62, 0x80
	v_lshrrev_b32_e32 v127, 8, v0
	v_or_b32_e32 v128, s20, v62
	v_mad_u32_u24 v129, v127, 7, 0
	v_add_u32_e32 v130, v128, v129
	v_sub_u32_e32 v129, v129, v1
	v_cmp_gt_u32_e64 s[58:59], 11, v129
	v_cmp_gt_u32_e64 s[60:61], s62, v130
	s_and_b64 s[44:45], s[58:59], s[60:61]
	v_mad_u32_u24 v129, v127, 7, 1
	v_add_u32_e32 v130, v128, v129
	v_sub_u32_e32 v129, v129, v1
	v_cmp_gt_u32_e64 s[58:59], 11, v129
	v_cmp_gt_u32_e64 s[60:61], s62, v130
	s_and_b64 s[46:47], s[58:59], s[60:61]
	v_mad_u32_u24 v129, v127, 7, 2
	v_add_u32_e32 v130, v128, v129
	v_sub_u32_e32 v129, v129, v1
	v_cmp_gt_u32_e64 s[58:59], 11, v129
	v_cmp_gt_u32_e64 s[60:61], s62, v130
	s_and_b64 s[48:49], s[58:59], s[60:61]
	v_mad_u32_u24 v129, v127, 7, 3
	v_add_u32_e32 v130, v128, v129
	v_sub_u32_e32 v129, v129, v1
	v_cmp_gt_u32_e64 s[58:59], 11, v129
	v_cmp_gt_u32_e64 s[60:61], s62, v130
	s_and_b64 s[50:51], s[58:59], s[60:61]
	v_mad_u32_u24 v129, v127, 7, 4
	v_add_u32_e32 v130, v128, v129
	v_sub_u32_e32 v129, v129, v1
	v_cmp_gt_u32_e64 s[58:59], 11, v129
	v_cmp_gt_u32_e64 s[60:61], s62, v130
	s_and_b64 s[52:53], s[58:59], s[60:61]
	v_mad_u32_u24 v129, v127, 7, 5
	v_add_u32_e32 v130, v128, v129
	v_sub_u32_e32 v129, v129, v1
	v_cmp_gt_u32_e64 s[58:59], 11, v129
	v_cmp_gt_u32_e64 s[60:61], s62, v130
	s_and_b64 s[54:55], s[58:59], s[60:61]
	v_mad_u32_u24 v129, v127, 7, 6
	v_add_u32_e32 v130, v128, v129
	v_sub_u32_e32 v129, v129, v1
	v_cmp_gt_u32_e64 s[58:59], 11, v129
	v_cmp_gt_u32_e64 s[60:61], s62, v130
	s_and_b64 s[56:57], s[58:59], s[60:61]
	v_mov_b32_e32 v52, 1
	v_lshlrev_b16_sdwa v52, v52, v65 dst_sel:DWORD dst_unused:UNUSED_PAD src0_sel:DWORD src1_sel:WORD_1
	v_mul_i32_i24_e32 v51, -9, v64
	v_add_u16_e32 v52, v52, v64
	v_mul_u32_u24_e32 v52, 0xa0, v52
	v_add_lshl_u32 v51, v51, v0, 4
	s_waitcnt vmcnt(9)
	v_cndmask_b32_e32 v29, 0, v29, vcc
	v_cndmask_b32_e32 v28, 0, v28, vcc
	v_cndmask_b32_e32 v27, 0, v27, vcc
	v_cndmask_b32_e32 v26, 0, v26, vcc
	v_add3_u32 v51, 0, v52, v51
	ds_write_b128 v51, v[26:29]
	v_lshlrev_b16_e32 v27, 1, v67
	v_mul_i32_i24_e32 v26, -9, v66
	v_add_u16_e32 v27, v27, v66
	v_mul_u32_u24_e32 v27, 0xa0, v27
	v_add_lshl_u32 v26, v26, v59, 4
	s_waitcnt vmcnt(8)
	v_cndmask_b32_e64 v33, 0, v33, s[2:3]
	v_cndmask_b32_e64 v32, 0, v32, s[2:3]
	v_cndmask_b32_e64 v31, 0, v31, s[2:3]
	v_cndmask_b32_e64 v30, 0, v30, s[2:3]
	v_add3_u32 v26, 0, v27, v26
	v_lshlrev_b16_e32 v27, 1, v69
	ds_write_b128 v26, v[30:33]
	v_mul_i32_i24_e32 v26, -9, v68
	v_add_u16_e32 v27, v27, v68
	v_mul_u32_u24_e32 v27, 0xa0, v27
	v_add_lshl_u32 v26, v26, v58, 4
	s_waitcnt vmcnt(7)
	v_cndmask_b32_e64 v37, 0, v37, s[4:5]
	v_cndmask_b32_e64 v36, 0, v36, s[4:5]
	v_cndmask_b32_e64 v35, 0, v35, s[4:5]
	v_cndmask_b32_e64 v34, 0, v34, s[4:5]
	v_add3_u32 v26, 0, v27, v26
	v_lshlrev_b16_e32 v27, 1, v72
	ds_write_b128 v26, v[34:37]
	v_mul_i32_i24_e32 v26, -9, v71
	v_add_u16_e32 v27, v27, v71
	v_mul_u32_u24_e32 v27, 0xa0, v27
	v_add_lshl_u32 v26, v26, v70, 4
	v_mul_u32_u24_e32 v28, 0xca5, v73
	s_waitcnt vmcnt(6)
	v_cndmask_b32_e64 v45, 0, v45, s[8:9]
	v_cndmask_b32_e64 v44, 0, v44, s[8:9]
	v_cndmask_b32_e64 v43, 0, v43, s[8:9]
	v_cndmask_b32_e64 v42, 0, v42, s[8:9]
	v_add3_u32 v26, 0, v27, v26
	v_lshrrev_b32_e32 v28, 18, v28
	ds_write_b128 v26, v[42:45]
	v_mul_u32_u24_e32 v27, 0x1c72, v73
	v_mov_b32_e32 v26, -9
	v_and_b32_e32 v28, 62, v28
	v_mul_i32_i24_sdwa v29, v27, v26 dst_sel:DWORD dst_unused:UNUSED_PAD src0_sel:WORD_1 src1_sel:DWORD
	v_add_u16_sdwa v27, v28, v27 dst_sel:DWORD dst_unused:UNUSED_PAD src0_sel:DWORD src1_sel:WORD_1
	v_mul_u32_u24_e32 v27, 0xa0, v27
	v_add_lshl_u32 v28, v29, v73, 4
	s_movk_i32 s2, 0x164
	v_bfe_u32 v50, v0, 4, 2
	s_waitcnt vmcnt(5)
	v_cndmask_b32_e64 v49, 0, v49, s[10:11]
	v_cndmask_b32_e64 v48, 0, v48, s[10:11]
	v_cndmask_b32_e64 v47, 0, v47, s[10:11]
	v_cndmask_b32_e64 v46, 0, v46, s[10:11]
	v_add3_u32 v27, 0, v27, v28
	v_cmp_gt_u32_e32 vcc, s2, v0
	ds_write_b128 v27, v[46:49]
	s_and_saveexec_b64 s[2:3], vcc
	s_cbranch_execz .LBB1_16
	v_mul_u32_u24_e32 v32, 0xca5, v74
	v_lshrrev_b32_e32 v32, 18, v32
	v_mul_u32_u24_e32 v27, 0x1c72, v74
	v_and_b32_e32 v32, 62, v32
	v_mul_i32_i24_sdwa v26, v27, v26 dst_sel:DWORD dst_unused:UNUSED_PAD src0_sel:WORD_1 src1_sel:DWORD
	v_add_u16_sdwa v27, v32, v27 dst_sel:DWORD dst_unused:UNUSED_PAD src0_sel:DWORD src1_sel:WORD_1
	v_mul_u32_u24_e32 v27, 0xa0, v27
	v_add_lshl_u32 v26, v26, v74, 4
	s_waitcnt vmcnt(4)
	v_cndmask_b32_e64 v31, 0, v41, s[6:7]
	v_cndmask_b32_e64 v30, 0, v40, s[6:7]
	v_cndmask_b32_e64 v29, 0, v39, s[6:7]
	v_cndmask_b32_e64 v28, 0, v38, s[6:7]
	v_add3_u32 v26, 0, v27, v26
	ds_write_b128 v26, v[28:31]
.LBB1_16:
	s_or_b64 exec, exec, s[2:3]
	s_movk_i32 s2, 0x168
	s_waitcnt vmcnt(4)
	v_and_b32_e32 v39, 63, v0
	v_and_b32_e32 v40, 15, v0
	v_lshlrev_b32_e32 v26, 3, v50
	v_cmp_gt_u32_e32 vcc, s2, v0
	s_and_saveexec_b64 s[2:3], vcc
	s_movk_i32 s4, 0xa0
	v_mad_u32_u24 v27, v0, s4, 0
	v_mov_b32_e32 v28, 0x3c00
	ds_write_b16 v27, v28 offset:144
	s_or_b64 exec, exec, s[2:3]
	v_lshlrev_b32_e32 v38, 2, v50
	v_or_b32_e32 v28, s21, v63
	v_add_u32_e32 v29, v28, v38
	v_sub_u32_e32 v30, v38, v61
	s_movk_i32 s7, 0x80
	v_cmp_gt_u32_e64 s[2:3], 11, v30
	v_cmp_gt_u32_e64 s[4:5], s7, v29
	v_or_b32_e32 v29, 1, v38
	s_and_b64 s[2:3], s[2:3], s[4:5]
	v_mov_b32_e32 v111, 0xff800000
	v_add_u32_e32 v30, v28, v29
	v_sub_u32_e32 v29, v29, v61
	v_cndmask_b32_e64 v112, v111, 0, s[2:3]
	v_cmp_gt_u32_e64 s[2:3], 11, v29
	v_cmp_gt_u32_e64 s[4:5], s7, v30
	v_or_b32_e32 v29, 2, v38
	v_lshrrev_b32_e32 v110, 8, v0
	s_and_b64 s[2:3], s[2:3], s[4:5]
	v_add_u32_e32 v30, v28, v29
	v_sub_u32_e32 v29, v29, v61
	v_cndmask_b32_e64 v113, v111, 0, s[2:3]
	v_cmp_gt_u32_e64 s[2:3], 11, v29
	v_or_b32_e32 v29, 3, v38
	v_mad_u32_u24 v41, v110, 7, v62
	v_cmp_gt_u32_e64 s[4:5], s7, v30
	v_add_u32_e32 v28, v28, v29
	v_mad_u32_u24 v98, v41, 20, v63
	s_and_b64 s[2:3], s[2:3], s[4:5]
	v_cmp_gt_u32_e64 s[4:5], s7, v28
	v_add_u32_e32 v28, v98, v40
	s_movk_i32 s6, 0xa0
	v_mul_lo_u32 v28, v28, s6
	v_add_u32_e32 v99, 0, v28
	v_mul_u32_u24_e32 v27, 7, v110
	v_sub_u32_e32 v29, v29, v61
	v_lshl_add_u32 v94, v26, 1, v99
	s_waitcnt lgkmcnt(0)
	s_barrier
	v_cndmask_b32_e64 v114, v111, 0, s[2:3]
	v_cmp_gt_u32_e64 s[2:3], 11, v29
	ds_read_b128 v[26:29], v94
	s_and_b64 s[2:3], s[2:3], s[4:5]
	ds_read_b128 v[34:37], v94 offset:64
	v_cndmask_b32_e64 v115, v111, 0, s[2:3]
	v_cndmask_b32_e64 v30, v111, v112, s[44:45]
	v_cndmask_b32_e64 v33, v111, v115, s[44:45]
	v_cndmask_b32_e64 v32, v111, v114, s[44:45]
	v_cndmask_b32_e64 v31, v111, v113, s[44:45]
	v_cmp_gt_u32_e32 vcc, 16, v39
	v_add_u32_e32 v98, v98, v38
	s_waitcnt lgkmcnt(1)
	v_mfma_f32_16x16x32_f16 v[30:33], v[26:29], v[10:13], v[30:33]
	ds_read_b128 v[42:45], v99 offset:128
	ds_read_b128 v[46:49], v94 offset:3200
	v_cndmask_b32_e32 v29, 0, v25, vcc
	s_waitcnt lgkmcnt(2)
	v_mfma_f32_16x16x32_f16 v[30:33], v[34:37], v[2:5], v[30:33]
	v_cndmask_b32_e32 v28, 0, v24, vcc
	v_cndmask_b32_e32 v27, 0, v23, vcc
	v_cndmask_b32_e32 v26, 0, v22, vcc
	ds_read_b128 v[34:37], v94 offset:3264
	ds_read_b128 v[50:53], v99 offset:3328
	s_waitcnt lgkmcnt(3)
	v_mfma_f32_16x16x32_f16 v[22:25], v[42:45], v[26:29], v[30:33]
	ds_read_b128 v[42:45], v94 offset:6400
	ds_read_b128 v[62:65], v94 offset:6464
	v_or_b32_e32 v98, v98, v1
	v_cndmask_b32_e64 v30, v111, v112, s[46:47]
	v_cndmask_b32_e64 v33, v111, v115, s[46:47]
	v_cndmask_b32_e64 v32, v111, v114, s[46:47]
	v_cndmask_b32_e64 v31, v111, v113, s[46:47]
	v_mul_lo_u32 v98, v98, s6
	v_lshlrev_b32_e32 v61, 3, v61
	s_waitcnt lgkmcnt(4)
	v_mfma_f32_16x16x32_f16 v[30:33], v[46:49], v[10:13], v[30:33]
	ds_read_b128 v[46:49], v99 offset:6528
	ds_read_b128 v[66:69], v94 offset:9600
	v_add3_u32 v61, 0, v98, v61
	s_waitcnt lgkmcnt(5)
	v_mfma_f32_16x16x32_f16 v[30:33], v[34:37], v[2:5], v[30:33]
	v_cndmask_b32_e64 v34, v111, v112, s[48:49]
	v_cndmask_b32_e64 v37, v111, v115, s[48:49]
	v_cndmask_b32_e64 v36, v111, v114, s[48:49]
	v_cndmask_b32_e64 v35, v111, v113, s[48:49]
	ds_read_b128 v[70:73], v94 offset:9664
	ds_read_b128 v[74:77], v99 offset:9728
	s_waitcnt lgkmcnt(6)
	v_mfma_f32_16x16x32_f16 v[30:33], v[50:53], v[26:29], v[30:33]
	ds_read_b128 v[50:53], v94 offset:12800
	ds_read_b128 v[78:81], v94 offset:12864
	s_waitcnt vmcnt(3)
	v_cvt_pk_f16_f32 v21, v20, v21
	s_waitcnt lgkmcnt(7)
	v_mfma_f32_16x16x32_f16 v[34:37], v[42:45], v[10:13], v[34:37]
	ds_read_b128 v[42:45], v99 offset:12928
	ds_read_b128 v[82:85], v94 offset:16000
	v_cvt_pk_f16_f32 v20, v18, v19
	s_waitcnt lgkmcnt(8)
	v_mfma_f32_16x16x32_f16 v[34:37], v[62:65], v[2:5], v[34:37]
	ds_read_b128 v[62:65], v94 offset:16064
	ds_read_b128 v[86:89], v99 offset:16128
	v_mul_u32_u24_e32 v18, 0xa0, v60
	s_waitcnt lgkmcnt(9)
	v_mfma_f32_16x16x32_f16 v[34:37], v[46:49], v[26:29], v[34:37]
	v_cndmask_b32_e64 v46, v111, v112, s[50:51]
	v_cndmask_b32_e64 v49, v111, v115, s[50:51]
	v_cndmask_b32_e64 v48, v111, v114, s[50:51]
	v_cndmask_b32_e64 v47, v111, v113, s[50:51]
	ds_read_b128 v[90:93], v94 offset:19200
	ds_read_b128 v[94:97], v94 offset:19264
	s_waitcnt lgkmcnt(10)
	v_mfma_f32_16x16x32_f16 v[46:49], v[66:69], v[10:13], v[46:49]
	ds_read_b128 v[66:69], v99 offset:19328
	ds_read_b64_tr_b16 v[100:101], v61 offset:3200
	v_lshlrev_b32_e32 v19, 1, v56
	s_waitcnt lgkmcnt(11)
	v_mfma_f32_16x16x32_f16 v[46:49], v[70:73], v[2:5], v[46:49]
	ds_read_b64_tr_b16 v[98:99], v61
	ds_read_b64_tr_b16 v[70:71], v61 offset:32
	s_waitcnt lgkmcnt(12)
	v_mfma_f32_16x16x32_f16 v[46:49], v[74:77], v[26:29], v[46:49]
	v_cndmask_b32_e64 v74, v111, v112, s[52:53]
	v_cndmask_b32_e64 v77, v111, v115, s[52:53]
	v_cndmask_b32_e64 v76, v111, v114, s[52:53]
	v_cndmask_b32_e64 v75, v111, v113, s[52:53]
	ds_read_b64_tr_b16 v[72:73], v61 offset:3232
	ds_read_b64_tr_b16 v[102:103], v61 offset:64
	s_waitcnt lgkmcnt(13)
	v_mfma_f32_16x16x32_f16 v[50:53], v[50:53], v[10:13], v[74:77]
	ds_read_b64_tr_b16 v[104:105], v61 offset:3264
	v_add3_u32 v18, 0, v18, v19
	s_movk_i32 s4, 0xe39
	ds_read_b64_tr_b16 v[74:75], v61 offset:96
	s_waitcnt lgkmcnt(14)
	v_mfma_f32_16x16x32_f16 v[50:53], v[78:81], v[2:5], v[50:53]
	ds_read_b64_tr_b16 v[76:77], v61 offset:3296
	ds_read_b64_tr_b16 v[78:79], v61 offset:128
	s_movk_i32 s5, 0xffee
	s_waitcnt lgkmcnt(14)
	v_mfma_f32_16x16x32_f16 v[42:45], v[42:45], v[26:29], v[50:53]
	ds_read_b64_tr_b16 v[80:81], v61 offset:3328
	ds_read_b64_tr_b16 v[106:107], v61 offset:6400
	s_waitcnt vmcnt(2)
	v_cvt_pk_f16_f32 v17, v16, v17
	v_cndmask_b32_e64 v50, v111, v112, s[54:55]
	v_cndmask_b32_e64 v53, v111, v115, s[54:55]
	v_cndmask_b32_e64 v52, v111, v114, s[54:55]
	v_cndmask_b32_e64 v51, v111, v113, s[54:55]
	v_cvt_pk_f16_f32 v16, v14, v15
	s_nop 0
	v_mfma_f32_16x16x32_f16 v[50:53], v[82:85], v[10:13], v[50:53]
	ds_read_b64_tr_b16 v[108:109], v61 offset:9600
	ds_read_b64_tr_b16 v[82:83], v61 offset:6432
	s_waitcnt lgkmcnt(14)
	v_mfma_f32_16x16x32_f16 v[50:53], v[62:65], v[2:5], v[50:53]
	ds_read_b64_tr_b16 v[84:85], v61 offset:9632
	ds_read_b64_tr_b16 v[62:63], v61 offset:6464
	v_mfma_f32_16x16x32_f16 v[50:53], v[86:89], v[26:29], v[50:53]
	v_cndmask_b32_e64 v86, v111, v112, s[56:57]
	v_cndmask_b32_e64 v89, v111, v115, s[56:57]
	v_cndmask_b32_e64 v88, v111, v114, s[56:57]
	v_cndmask_b32_e64 v87, v111, v113, s[56:57]
	ds_read_b64_tr_b16 v[64:65], v61 offset:9664
	ds_read_b64_tr_b16 v[110:111], v61 offset:6496
	v_mfma_f32_16x16x32_f16 v[10:13], v[90:93], v[10:13], v[86:89]
	s_mov_b32 s2, 0xff800000
	ds_read_b64_tr_b16 v[112:113], v61 offset:9696
	s_nop 0
	ds_read_b64_tr_b16 v[86:87], v61 offset:6528
	v_mfma_f32_16x16x32_f16 v[2:5], v[94:97], v[2:5], v[10:13]
	ds_read_b64_tr_b16 v[88:89], v61 offset:9728
	s_nop 1
	v_max3_f32 v12, v22, s2, v23
	v_max3_f32 v12, v12, v24, v25
	v_max3_f32 v12, v12, v30, v31
	v_max3_f32 v12, v12, v32, v33
	v_max3_f32 v12, v12, v34, v35
	v_max3_f32 v12, v12, v36, v37
	v_max3_f32 v12, v12, v46, v47
	v_max3_f32 v12, v12, v48, v49
	v_mbcnt_lo_u32_b32 v13, -1, 0
	ds_read_b64_tr_b16 v[10:11], v61 offset:12800
	s_waitcnt lgkmcnt(14)
	v_mfma_f32_16x16x32_f16 v[2:5], v[66:69], v[26:29], v[2:5]
	v_max3_f32 v12, v12, v42, v43
	v_mbcnt_hi_u32_b32 v13, -1, v13
	v_max3_f32 v12, v12, v44, v45
	v_and_b32_e32 v27, 64, v13
	v_max3_f32 v12, v12, v50, v51
	v_xor_b32_e32 v26, 16, v13
	v_add_u32_e32 v27, 64, v27
	v_max3_f32 v12, v12, v52, v53
	v_cmp_lt_i32_e32 vcc, v26, v27
	v_max3_f32 v12, v12, v2, v3
	v_max3_f32 v12, v12, v4, v5
	v_mov_b32_e32 v26, v12
	s_load_dwordx2 s[2:3], s[0:1], 0x20
	s_movk_i32 s0, 0x510
	v_permlane16_swap_b32_e32 v12, v26
	v_cmp_gt_u32_e32 vcc, 11, v41
	v_mov_b32_e32 v41, 0xc80
	v_max_f32_e32 v12, v12, v26
	v_mov_b32_e32 v13, v12
	s_nop 1
	v_permlane32_swap_b32_e32 v12, v13
	s_waitcnt lgkmcnt(0)
	s_nop 0
	v_max_f32_e32 v26, v12, v13
	v_sub_f32_e32 v29, v34, v26
	v_exp_f32_e32 v92, v29
	v_sub_f32_e32 v29, v35, v26
	v_exp_f32_e32 v93, v29
	v_sub_f32_e32 v29, v36, v26
	v_exp_f32_e32 v36, v29
	v_sub_f32_e32 v29, v37, v26
	v_exp_f32_e32 v37, v29
	v_sub_f32_e32 v29, v46, v26
	v_exp_f32_e32 v94, v29
	v_sub_f32_e32 v29, v47, v26
	v_exp_f32_e32 v95, v29
	v_sub_f32_e32 v29, v48, v26
	v_sub_f32_e32 v13, v23, v26
	v_sub_f32_e32 v23, v25, v26
	v_sub_f32_e32 v25, v31, v26
	v_exp_f32_e32 v96, v29
	v_sub_f32_e32 v29, v49, v26
	v_sub_f32_e32 v12, v22, v26
	v_sub_f32_e32 v22, v24, v26
	v_sub_f32_e32 v24, v30, v26
	v_exp_f32_e32 v27, v25
	v_sub_f32_e32 v25, v32, v26
	v_sub_f32_e32 v28, v33, v26
	v_exp_f32_e32 v97, v29
	v_sub_f32_e32 v29, v42, v26
	v_exp_f32_e32 v12, v12
	v_exp_f32_e32 v13, v13
	v_exp_f32_e32 v22, v22
	v_exp_f32_e32 v23, v23
	v_exp_f32_e32 v24, v24
	v_exp_f32_e32 v25, v25
	v_exp_f32_e32 v28, v28
	v_exp_f32_e32 v114, v29
	v_sub_f32_e32 v29, v43, v26
	v_exp_f32_e32 v115, v29
	v_sub_f32_e32 v29, v44, v26
	v_exp_f32_e32 v116, v29
	v_sub_f32_e32 v29, v45, v26
	v_exp_f32_e32 v117, v29
	v_sub_f32_e32 v29, v50, v26
	v_exp_f32_e32 v118, v29
	v_sub_f32_e32 v29, v51, v26
	v_cvt_pk_f16_f32 v25, v25, v28
	v_cvt_pk_f16_f32 v24, v24, v27
	v_cvt_pk_f16_f32 v23, v22, v23
	v_cvt_pk_f16_f32 v22, v12, v13
	v_exp_f32_e32 v119, v29
	v_cndmask_b32_e32 v41, 0, v41, vcc
	v_mfma_f32_16x16x32_f16 v[28:31], v[98:101], v[22:25], 0
	ds_read_b64_tr_b16 v[12:13], v61 offset:16000
	ds_read_b64_tr_b16 v[32:33], v61 offset:12832
	v_sub_f32_e32 v27, v52, v26
	v_mfma_f32_16x16x32_f16 v[42:45], v[70:73], v[22:25], 0
	ds_read_b64_tr_b16 v[34:35], v61 offset:16032
	ds_read_b64_tr_b16 v[46:47], v61 offset:12864
	v_exp_f32_e32 v27, v27
	v_mfma_f32_16x16x32_f16 v[66:69], v[102:105], v[22:25], 0
	ds_read_b64_tr_b16 v[48:49], v61 offset:16064
	ds_read_b64_tr_b16 v[70:71], v61 offset:12896
	v_sub_f32_e32 v2, v2, v26
	v_mfma_f32_16x16x32_f16 v[74:77], v[74:77], v[22:25], 0
	ds_read_b64_tr_b16 v[72:73], v61 offset:16096
	ds_read_b64_tr_b16 v[90:91], v61 offset:12928
	v_cmp_gt_u32_e32 vcc, s0, v58
	v_mfma_f32_16x16x32_f16 v[22:25], v[78:81], v[22:25], 0
	v_cvt_pk_f16_f32 v78, v92, v93
	ds_read_b64_tr_b16 v[92:93], v61 offset:16128
	v_cvt_pk_f16_f32 v81, v96, v97
	v_cvt_pk_f16_f32 v80, v94, v95
	v_cvt_pk_f16_f32 v79, v36, v37
	v_add_u32_e32 v36, v61, v41
	v_sub_f32_e32 v37, v53, v26
	ds_read_b64_tr_b16 v[94:95], v61 offset:19200
	v_mfma_f32_16x16x32_f16 v[28:31], v[106:109], v[78:81], v[28:31]
	ds_read_b64_tr_b16 v[96:97], v36 offset:19200
	ds_read_b64_tr_b16 v[100:101], v36 offset:19232
	v_exp_f32_e32 v37, v37
	v_mfma_f32_16x16x32_f16 v[42:45], v[82:85], v[78:81], v[42:45]
	ds_read_b64_tr_b16 v[98:99], v61 offset:19232
	ds_read_b64_tr_b16 v[50:51], v61 offset:19264
	v_mfma_f32_16x16x32_f16 v[62:65], v[62:65], v[78:81], v[66:69]
	ds_read_b64_tr_b16 v[52:53], v36 offset:19264
	s_nop 1
	ds_read_b64_tr_b16 v[66:67], v61 offset:19296
	v_mfma_f32_16x16x32_f16 v[74:77], v[110:113], v[78:81], v[74:77]
	ds_read_b64_tr_b16 v[68:69], v36 offset:19296
	ds_read_b64_tr_b16 v[82:83], v61 offset:19328
	v_mfma_f32_16x16x32_f16 v[22:25], v[86:89], v[78:81], v[22:25]
	ds_read_b64_tr_b16 v[84:85], v36 offset:19328
	ds_write_b64 v18, v[20:21] offset:57600
	v_mul_u32_u24_sdwa v18, v59, s4 dst_sel:DWORD dst_unused:UNUSED_PAD src0_sel:WORD_0 src1_sel:DWORD
	v_mul_i32_i24_sdwa v19, v18, s5 dst_sel:DWORD dst_unused:UNUSED_PAD src0_sel:WORD_1 src1_sel:DWORD
	v_mul_u32_u24_sdwa v14, v18, s6 dst_sel:DWORD dst_unused:UNUSED_PAD src0_sel:WORD_1 src1_sel:DWORD
	v_add_lshl_u32 v15, v19, v59, 3
	v_exp_f32_e32 v18, v2
	v_sub_f32_e32 v19, v3, v26
	v_sub_f32_e32 v2, v4, v26
	v_sub_f32_e32 v21, v5, v26
	v_cvt_pk_f16_f32 v81, v27, v37
	v_cvt_pk_f16_f32 v80, v118, v119
	v_cvt_pk_f16_f32 v79, v116, v117
	v_cvt_pk_f16_f32 v78, v114, v115
	v_add3_u32 v14, 0, v14, v15
	v_exp_f32_e32 v20, v2
	v_exp_f32_e32 v21, v21
	v_exp_f32_e32 v19, v19
	s_waitcnt lgkmcnt(14)
	v_mfma_f32_16x16x32_f16 v[10:13], v[10:13], v[78:81], v[28:31]
	ds_write_b64 v14, v[16:17] offset:57600
	v_mfma_f32_16x16x32_f16 v[14:17], v[32:35], v[78:81], v[42:45]
	v_mfma_f32_16x16x32_f16 v[28:31], v[46:49], v[78:81], v[62:65]
	s_nop 1
	v_mov_b32_e32 v44, 0
	v_cvt_pk_f16_f32 v43, v20, v21
	v_cvt_pk_f16_f32 v42, v18, v19
	s_waitcnt lgkmcnt(14)
	v_mfma_f32_16x16x32_f16 v[2:5], v[70:73], v[78:81], v[74:77]
	v_mov_b32_e32 v45, v44
	s_waitcnt lgkmcnt(12)
	v_mfma_f32_16x16x32_f16 v[32:35], v[90:93], v[78:81], v[22:25]
	s_waitcnt lgkmcnt(10)
	v_mfma_f32_16x16x32_f16 v[22:25], v[94:97], v[42:45], v[10:13]
	s_waitcnt lgkmcnt(8)
	v_mfma_f32_16x16x32_f16 v[18:21], v[98:101], v[42:45], v[14:17]
	s_waitcnt lgkmcnt(6)
	v_mfma_f32_16x16x32_f16 v[14:17], v[50:53], v[42:45], v[28:31]
	s_waitcnt lgkmcnt(4)
	v_mfma_f32_16x16x32_f16 v[10:13], v[66:69], v[42:45], v[2:5]
	s_waitcnt lgkmcnt(2)
	v_mfma_f32_16x16x32_f16 v[2:5], v[82:85], v[42:45], v[32:35]
	s_and_saveexec_b64 s[0:1], vcc
	s_cbranch_execz .LBB1_20
	v_mul_u32_u24_sdwa v27, v58, s4 dst_sel:DWORD dst_unused:UNUSED_PAD src0_sel:WORD_0 src1_sel:DWORD
	v_mul_i32_i24_sdwa v28, v27, s5 dst_sel:DWORD dst_unused:UNUSED_PAD src0_sel:WORD_1 src1_sel:DWORD
	s_waitcnt vmcnt(1)
	v_cvt_pk_f16_f32 v9, v8, v9
	v_cvt_pk_f16_f32 v8, v6, v7
	v_mul_u32_u24_sdwa v6, v27, s6 dst_sel:DWORD dst_unused:UNUSED_PAD src0_sel:WORD_1 src1_sel:DWORD
	v_add_lshl_u32 v7, v28, v58, 3
	v_add3_u32 v6, 0, v6, v7
	ds_write_b64 v6, v[8:9] offset:57600

.LBB2_14:
	s_or_b64 exec, exec, s[14:15]
	s_movk_i32 s62, 0x80
	v_lshrrev_b32_e32 v144, 8, v0
	v_or_b32_e32 v145, s29, v76
	v_mad_u32_u24 v146, v144, 7, 0
	v_add_u32_e32 v147, v145, v146
	v_sub_u32_e32 v146, v146, v60
	v_cmp_gt_u32_e64 s[58:59], 11, v146
	v_cmp_gt_u32_e64 s[60:61], s62, v147
	s_and_b64 s[44:45], s[58:59], s[60:61]
	v_mad_u32_u24 v146, v144, 7, 1
	v_add_u32_e32 v147, v145, v146
	v_sub_u32_e32 v146, v146, v60
	v_cmp_gt_u32_e64 s[58:59], 11, v146
	v_cmp_gt_u32_e64 s[60:61], s62, v147
	s_and_b64 s[46:47], s[58:59], s[60:61]
	v_mad_u32_u24 v146, v144, 7, 2
	v_add_u32_e32 v147, v145, v146
	v_sub_u32_e32 v146, v146, v60
	v_cmp_gt_u32_e64 s[58:59], 11, v146
	v_cmp_gt_u32_e64 s[60:61], s62, v147
	s_and_b64 s[48:49], s[58:59], s[60:61]
	v_mad_u32_u24 v146, v144, 7, 3
	v_add_u32_e32 v147, v145, v146
	v_sub_u32_e32 v146, v146, v60
	v_cmp_gt_u32_e64 s[58:59], 11, v146
	v_cmp_gt_u32_e64 s[60:61], s62, v147
	s_and_b64 s[50:51], s[58:59], s[60:61]
	v_mad_u32_u24 v146, v144, 7, 4
	v_add_u32_e32 v147, v145, v146
	v_sub_u32_e32 v146, v146, v60
	v_cmp_gt_u32_e64 s[58:59], 11, v146
	v_cmp_gt_u32_e64 s[60:61], s62, v147
	s_and_b64 s[52:53], s[58:59], s[60:61]
	v_mad_u32_u24 v146, v144, 7, 5
	v_add_u32_e32 v147, v145, v146
	v_sub_u32_e32 v146, v146, v60
	v_cmp_gt_u32_e64 s[58:59], 11, v146
	v_cmp_gt_u32_e64 s[60:61], s62, v147
	s_and_b64 s[54:55], s[58:59], s[60:61]
	v_mad_u32_u24 v146, v144, 7, 6
	v_add_u32_e32 v147, v145, v146
	v_sub_u32_e32 v146, v146, v60
	v_cmp_gt_u32_e64 s[58:59], 11, v146
	v_cmp_gt_u32_e64 s[60:61], s62, v147
	s_and_b64 s[56:57], s[58:59], s[60:61]
	v_mov_b32_e32 v52, 1
	v_lshlrev_b16_sdwa v52, v52, v78 dst_sel:DWORD dst_unused:UNUSED_PAD src0_sel:DWORD src1_sel:WORD_1
	v_mul_i32_i24_e32 v51, -9, v77
	v_add_u16_e32 v52, v52, v77
	v_mul_u32_u24_e32 v52, 0xa0, v52
	v_add_lshl_u32 v51, v51, v0, 4
	s_waitcnt vmcnt(17)
	v_cndmask_b32_e32 v29, 0, v29, vcc
	v_cndmask_b32_e32 v28, 0, v28, vcc
	v_cndmask_b32_e32 v27, 0, v27, vcc
	v_cndmask_b32_e32 v26, 0, v26, vcc
	v_add3_u32 v51, 0, v52, v51
	ds_write_b128 v51, v[26:29]
	v_lshlrev_b16_e32 v27, 1, v80
	v_mul_i32_i24_e32 v26, -9, v79
	v_add_u16_e32 v27, v27, v79
	v_mul_u32_u24_e32 v27, 0xa0, v27
	v_add_lshl_u32 v26, v26, v62, 4
	s_waitcnt vmcnt(16)
	v_cndmask_b32_e64 v33, 0, v33, s[2:3]
	v_cndmask_b32_e64 v32, 0, v32, s[2:3]
	v_cndmask_b32_e64 v31, 0, v31, s[2:3]
	v_cndmask_b32_e64 v30, 0, v30, s[2:3]
	v_add3_u32 v26, 0, v27, v26
	v_lshlrev_b16_e32 v27, 1, v82
	ds_write_b128 v26, v[30:33]
	v_mul_i32_i24_e32 v26, -9, v81
	v_add_u16_e32 v27, v27, v81
	v_mul_u32_u24_e32 v27, 0xa0, v27
	v_add_lshl_u32 v26, v26, v61, 4
	s_waitcnt vmcnt(15)
	v_cndmask_b32_e64 v37, 0, v37, s[4:5]
	v_cndmask_b32_e64 v36, 0, v36, s[4:5]
	v_cndmask_b32_e64 v35, 0, v35, s[4:5]
	v_cndmask_b32_e64 v34, 0, v34, s[4:5]
	v_add3_u32 v26, 0, v27, v26
	v_lshlrev_b16_e32 v27, 1, v85
	ds_write_b128 v26, v[34:37]
	v_mul_i32_i24_e32 v26, -9, v84
	v_add_u16_e32 v27, v27, v84
	v_mul_u32_u24_e32 v27, 0xa0, v27
	v_add_lshl_u32 v26, v26, v83, 4
	v_mul_u32_u24_e32 v28, 0xca5, v86
	s_waitcnt vmcnt(14)
	v_cndmask_b32_e64 v45, 0, v45, s[8:9]
	v_cndmask_b32_e64 v44, 0, v44, s[8:9]
	v_cndmask_b32_e64 v43, 0, v43, s[8:9]
	v_cndmask_b32_e64 v42, 0, v42, s[8:9]
	v_add3_u32 v26, 0, v27, v26
	v_lshrrev_b32_e32 v28, 18, v28
	ds_write_b128 v26, v[42:45]
	v_mul_u32_u24_e32 v27, 0x1c72, v86
	v_mov_b32_e32 v26, -9
	v_and_b32_e32 v28, 62, v28
	v_mul_i32_i24_sdwa v29, v27, v26 dst_sel:DWORD dst_unused:UNUSED_PAD src0_sel:WORD_1 src1_sel:DWORD
	v_add_u16_sdwa v27, v28, v27 dst_sel:DWORD dst_unused:UNUSED_PAD src0_sel:DWORD src1_sel:WORD_1
	v_mul_u32_u24_e32 v27, 0xa0, v27
	v_add_lshl_u32 v28, v29, v86, 4
	s_movk_i32 s2, 0x164
	v_bfe_u32 v50, v0, 4, 2
	s_waitcnt vmcnt(13)
	v_cndmask_b32_e64 v49, 0, v49, s[10:11]
	v_cndmask_b32_e64 v48, 0, v48, s[10:11]
	v_cndmask_b32_e64 v47, 0, v47, s[10:11]
	v_cndmask_b32_e64 v46, 0, v46, s[10:11]
	v_add3_u32 v27, 0, v27, v28
	v_cmp_gt_u32_e32 vcc, s2, v0
	ds_write_b128 v27, v[46:49]
	s_and_saveexec_b64 s[2:3], vcc
	s_cbranch_execz .LBB2_16
	v_mul_u32_u24_e32 v32, 0xca5, v87
	v_lshrrev_b32_e32 v32, 18, v32
	v_mul_u32_u24_e32 v27, 0x1c72, v87
	v_and_b32_e32 v32, 62, v32
	v_mul_i32_i24_sdwa v26, v27, v26 dst_sel:DWORD dst_unused:UNUSED_PAD src0_sel:WORD_1 src1_sel:DWORD
	v_add_u16_sdwa v27, v32, v27 dst_sel:DWORD dst_unused:UNUSED_PAD src0_sel:DWORD src1_sel:WORD_1
	v_mul_u32_u24_e32 v27, 0xa0, v27
	v_add_lshl_u32 v26, v26, v87, 4
	s_waitcnt vmcnt(12)
	v_cndmask_b32_e64 v31, 0, v41, s[6:7]
	v_cndmask_b32_e64 v30, 0, v40, s[6:7]
	v_cndmask_b32_e64 v29, 0, v39, s[6:7]
	v_cndmask_b32_e64 v28, 0, v38, s[6:7]
	v_add3_u32 v26, 0, v27, v26
	ds_write_b128 v26, v[28:31]
.LBB2_16:
	s_or_b64 exec, exec, s[2:3]
	s_movk_i32 s2, 0x168
	s_waitcnt vmcnt(12)
	v_and_b32_e32 v38, 63, v0
	v_lshlrev_b32_e32 v26, 3, v50
	v_cmp_gt_u32_e32 vcc, s2, v0
	s_and_saveexec_b64 s[2:3], vcc
	s_movk_i32 s4, 0xa0
	v_mad_u32_u24 v27, v0, s4, 0
	v_mov_b32_e32 v28, 0x3c00
	ds_write_b16 v27, v28 offset:144
	s_or_b64 exec, exec, s[2:3]
	v_lshlrev_b32_e32 v39, 2, v50
	v_or_b32_e32 v28, s30, v57
	v_add_u32_e32 v29, v28, v39
	v_sub_u32_e32 v30, v39, v1
	s_movk_i32 s7, 0x80
	v_cmp_gt_u32_e64 s[2:3], 11, v30
	v_cmp_gt_u32_e64 s[4:5], s7, v29
	v_or_b32_e32 v29, 1, v39
	s_and_b64 s[2:3], s[2:3], s[4:5]
	v_mov_b32_e32 v51, 0xff800000
	v_add_u32_e32 v30, v28, v29
	v_sub_u32_e32 v29, v29, v1
	v_cndmask_b32_e64 v52, v51, 0, s[2:3]
	v_cmp_gt_u32_e64 s[2:3], 11, v29
	v_cmp_gt_u32_e64 s[4:5], s7, v30
	v_or_b32_e32 v29, 2, v39
	v_lshrrev_b32_e32 v41, 8, v0
	s_and_b64 s[2:3], s[2:3], s[4:5]
	v_add_u32_e32 v30, v28, v29
	v_sub_u32_e32 v29, v29, v1
	v_cndmask_b32_e64 v53, v51, 0, s[2:3]
	v_cmp_gt_u32_e64 s[2:3], 11, v29
	v_or_b32_e32 v29, 3, v39
	v_mad_u32_u24 v40, v41, 7, v76
	v_cmp_gt_u32_e64 s[4:5], s7, v30
	v_add_u32_e32 v28, v28, v29
	v_mad_u32_u24 v116, v40, 20, v57
	s_and_b64 s[2:3], s[2:3], s[4:5]
	v_cmp_gt_u32_e64 s[4:5], s7, v28
	v_add_u32_e32 v28, v116, v59
	s_movk_i32 s6, 0xa0
	v_mul_lo_u32 v28, v28, s6
	v_add_u32_e32 v117, 0, v28
	v_mul_u32_u24_e32 v27, 7, v41
	v_sub_u32_e32 v29, v29, v1
	v_lshl_add_u32 v112, v26, 1, v117
	s_waitcnt lgkmcnt(0)
	s_barrier
	v_cndmask_b32_e64 v128, v51, 0, s[2:3]
	v_cmp_gt_u32_e64 s[2:3], 11, v29
	ds_read_b128 v[26:29], v112
	s_and_b64 s[2:3], s[2:3], s[4:5]
	ds_read_b128 v[34:37], v112 offset:64
	v_cndmask_b32_e64 v129, v51, 0, s[2:3]
	v_cndmask_b32_e64 v30, v51, v52, s[44:45]
	v_cndmask_b32_e64 v33, v51, v129, s[44:45]
	v_cndmask_b32_e64 v32, v51, v128, s[44:45]
	v_cndmask_b32_e64 v31, v51, v53, s[44:45]
	v_cmp_gt_u32_e32 vcc, 16, v38
	v_add_u32_e32 v116, v116, v39
	s_waitcnt lgkmcnt(1)
	v_mfma_f32_16x16x32_f16 v[30:33], v[26:29], v[10:13], v[30:33]
	ds_read_b128 v[42:45], v117 offset:128
	ds_read_b128 v[46:49], v112 offset:3200
	v_cndmask_b32_e32 v29, 0, v25, vcc
	s_waitcnt lgkmcnt(2)
	v_mfma_f32_16x16x32_f16 v[30:33], v[34:37], v[2:5], v[30:33]
	v_cndmask_b32_e32 v28, 0, v24, vcc
	v_cndmask_b32_e32 v27, 0, v23, vcc
	v_cndmask_b32_e32 v26, 0, v22, vcc
	ds_read_b128 v[34:37], v112 offset:3264
	ds_read_b128 v[76:79], v117 offset:3328
	s_waitcnt lgkmcnt(3)
	v_mfma_f32_16x16x32_f16 v[22:25], v[42:45], v[26:29], v[30:33]
	ds_read_b128 v[42:45], v112 offset:6400
	ds_read_b128 v[80:83], v112 offset:6464
	v_or_b32_e32 v116, v116, v60
	v_cndmask_b32_e64 v30, v51, v52, s[46:47]
	v_cndmask_b32_e64 v33, v51, v129, s[46:47]
	v_cndmask_b32_e64 v32, v51, v128, s[46:47]
	v_cndmask_b32_e64 v31, v51, v53, s[46:47]
	v_mul_lo_u32 v116, v116, s6
	s_waitcnt vmcnt(11)
	v_cvt_pk_f16_f32 v21, v20, v21
	s_waitcnt lgkmcnt(4)
	v_mfma_f32_16x16x32_f16 v[30:33], v[46:49], v[10:13], v[30:33]
	ds_read_b128 v[46:49], v117 offset:6528
	ds_read_b128 v[84:87], v112 offset:9600
	v_cvt_pk_f16_f32 v20, v18, v19
	s_waitcnt lgkmcnt(5)
	v_mfma_f32_16x16x32_f16 v[30:33], v[34:37], v[2:5], v[30:33]
	v_cndmask_b32_e64 v34, v51, v52, s[48:49]
	v_cndmask_b32_e64 v37, v51, v129, s[48:49]
	v_cndmask_b32_e64 v36, v51, v128, s[48:49]
	v_cndmask_b32_e64 v35, v51, v53, s[48:49]
	ds_read_b128 v[88:91], v112 offset:9664
	ds_read_b128 v[92:95], v117 offset:9728
	s_waitcnt lgkmcnt(6)
	v_mfma_f32_16x16x32_f16 v[30:33], v[76:79], v[26:29], v[30:33]
	ds_read_b128 v[76:79], v112 offset:12800
	ds_read_b128 v[96:99], v112 offset:12864
	v_mul_u32_u24_e32 v18, 0xa0, v75
	s_waitcnt lgkmcnt(7)
	v_mfma_f32_16x16x32_f16 v[34:37], v[42:45], v[10:13], v[34:37]
	ds_read_b128 v[42:45], v117 offset:12928
	ds_read_b128 v[100:103], v112 offset:16000
	v_lshlrev_b32_e32 v19, 1, v54
	s_waitcnt lgkmcnt(8)
	v_mfma_f32_16x16x32_f16 v[34:37], v[80:83], v[2:5], v[34:37]
	ds_read_b128 v[80:83], v112 offset:16064
	ds_read_b128 v[104:107], v117 offset:16128
	v_add3_u32 v18, 0, v18, v19
	s_waitcnt lgkmcnt(9)
	v_mfma_f32_16x16x32_f16 v[34:37], v[46:49], v[26:29], v[34:37]
	v_cndmask_b32_e64 v46, v51, v52, s[50:51]
	v_cndmask_b32_e64 v49, v51, v129, s[50:51]
	v_cndmask_b32_e64 v48, v51, v128, s[50:51]
	v_cndmask_b32_e64 v47, v51, v53, s[50:51]
	ds_read_b128 v[108:111], v112 offset:19200
	ds_read_b128 v[112:115], v112 offset:19264
	s_waitcnt lgkmcnt(10)
	v_mfma_f32_16x16x32_f16 v[46:49], v[84:87], v[10:13], v[46:49]
	ds_read_b128 v[84:87], v117 offset:19328
	v_lshlrev_b32_e32 v117, 3, v1
	v_add3_u32 v132, 0, v116, v117
	ds_read_b64_tr_b16 v[118:119], v132 offset:3200
	s_waitcnt lgkmcnt(11)
	v_mfma_f32_16x16x32_f16 v[46:49], v[88:91], v[2:5], v[46:49]
	ds_read_b64_tr_b16 v[116:117], v132
	ds_read_b64_tr_b16 v[88:89], v132 offset:32
	s_waitcnt lgkmcnt(12)
	v_mfma_f32_16x16x32_f16 v[46:49], v[92:95], v[26:29], v[46:49]
	v_cndmask_b32_e64 v92, v51, v52, s[52:53]
	v_cndmask_b32_e64 v95, v51, v129, s[52:53]
	v_cndmask_b32_e64 v94, v51, v128, s[52:53]
	v_cndmask_b32_e64 v93, v51, v53, s[52:53]
	ds_read_b64_tr_b16 v[90:91], v132 offset:3232
	ds_read_b64_tr_b16 v[120:121], v132 offset:64
	s_waitcnt lgkmcnt(13)
	v_mfma_f32_16x16x32_f16 v[76:79], v[76:79], v[10:13], v[92:95]
	ds_read_b64_tr_b16 v[122:123], v132 offset:3264
	s_movk_i32 s8, 0xffee
	s_waitcnt vmcnt(10)
	v_cvt_pk_f16_f32 v17, v16, v17
	ds_read_b64_tr_b16 v[92:93], v132 offset:96
	s_waitcnt lgkmcnt(14)
	v_mfma_f32_16x16x32_f16 v[76:79], v[96:99], v[2:5], v[76:79]
	ds_read_b64_tr_b16 v[94:95], v132 offset:3296
	ds_read_b64_tr_b16 v[96:97], v132 offset:128
	v_cvt_pk_f16_f32 v16, v14, v15
	s_waitcnt lgkmcnt(14)
	v_mfma_f32_16x16x32_f16 v[42:45], v[42:45], v[26:29], v[76:79]
	ds_read_b64_tr_b16 v[98:99], v132 offset:3328
	ds_read_b64_tr_b16 v[124:125], v132 offset:6400
	s_movk_i32 s4, 0x510
	v_cndmask_b32_e64 v76, v51, v52, s[54:55]
	v_cndmask_b32_e64 v79, v51, v129, s[54:55]
	v_cndmask_b32_e64 v78, v51, v128, s[54:55]
	v_cndmask_b32_e64 v77, v51, v53, s[54:55]
	s_nop 0
	v_mfma_f32_16x16x32_f16 v[76:79], v[100:103], v[10:13], v[76:79]
	ds_read_b64_tr_b16 v[126:127], v132 offset:9600
	ds_read_b64_tr_b16 v[100:101], v132 offset:6432
	s_waitcnt lgkmcnt(14)
	v_mfma_f32_16x16x32_f16 v[76:79], v[80:83], v[2:5], v[76:79]
	ds_read_b64_tr_b16 v[102:103], v132 offset:9632
	ds_read_b64_tr_b16 v[80:81], v132 offset:6464
	v_mfma_f32_16x16x32_f16 v[76:79], v[104:107], v[26:29], v[76:79]
	v_cndmask_b32_e64 v104, v51, v52, s[56:57]
	v_cndmask_b32_e64 v107, v51, v129, s[56:57]
	v_cndmask_b32_e64 v106, v51, v128, s[56:57]
	v_cndmask_b32_e64 v105, v51, v53, s[56:57]
	ds_read_b64_tr_b16 v[82:83], v132 offset:9664
	ds_read_b64_tr_b16 v[128:129], v132 offset:6496
	v_mfma_f32_16x16x32_f16 v[10:13], v[108:111], v[10:13], v[104:107]
	s_mov_b32 s2, 0xff800000
	ds_read_b64_tr_b16 v[130:131], v132 offset:9696
	s_movk_i32 s7, 0xe39
	ds_read_b64_tr_b16 v[104:105], v132 offset:6528
	v_mfma_f32_16x16x32_f16 v[2:5], v[112:115], v[2:5], v[10:13]
	ds_read_b64_tr_b16 v[106:107], v132 offset:9728
	s_nop 1
	v_max3_f32 v12, v22, s2, v23
	v_max3_f32 v12, v12, v24, v25
	v_max3_f32 v12, v12, v30, v31
	v_max3_f32 v12, v12, v32, v33
	v_max3_f32 v12, v12, v34, v35
	v_max3_f32 v12, v12, v36, v37
	v_max3_f32 v12, v12, v46, v47
	v_max3_f32 v12, v12, v48, v49
	v_mbcnt_lo_u32_b32 v13, -1, 0
	ds_read_b64_tr_b16 v[10:11], v132 offset:12800
	s_waitcnt lgkmcnt(14)
	v_mfma_f32_16x16x32_f16 v[2:5], v[84:87], v[26:29], v[2:5]
	v_max3_f32 v12, v12, v42, v43
	v_mbcnt_hi_u32_b32 v13, -1, v13
	v_max3_f32 v12, v12, v44, v45
	v_and_b32_e32 v27, 64, v13
	v_max3_f32 v12, v12, v76, v77
	v_xor_b32_e32 v26, 16, v13
	v_add_u32_e32 v27, 64, v27
	v_max3_f32 v12, v12, v78, v79
	v_cmp_lt_i32_e32 vcc, v26, v27
	v_max3_f32 v12, v12, v2, v3
	v_max3_f32 v12, v12, v4, v5
	v_mov_b32_e32 v26, v12
	v_cmp_lt_u32_e64 s[2:3], 15, v38
	s_nop 0
	v_permlane16_swap_b32_e32 v12, v26
	v_cmp_gt_u32_e32 vcc, 11, v40
	s_nop 0
	v_max_f32_e32 v12, v12, v26
	v_mov_b32_e32 v13, v12
	s_nop 1
	v_permlane32_swap_b32_e32 v12, v13
	s_waitcnt lgkmcnt(0)
	s_nop 0
	v_max_f32_e32 v28, v12, v13
	v_sub_f32_e32 v12, v22, v28
	v_sub_f32_e32 v22, v24, v28
	v_sub_f32_e32 v24, v30, v28
	v_sub_f32_e32 v30, v35, v28
	v_exp_f32_e32 v41, v30
	v_sub_f32_e32 v30, v36, v28
	v_exp_f32_e32 v51, v30
	v_sub_f32_e32 v30, v37, v28
	v_exp_f32_e32 v52, v30
	v_sub_f32_e32 v30, v46, v28
	v_exp_f32_e32 v53, v30
	v_sub_f32_e32 v30, v47, v28
	v_exp_f32_e32 v110, v30
	v_sub_f32_e32 v30, v48, v28
	v_sub_f32_e32 v13, v23, v28
	v_sub_f32_e32 v23, v25, v28
	v_sub_f32_e32 v25, v31, v28
	v_exp_f32_e32 v111, v30
	v_sub_f32_e32 v30, v49, v28
	v_exp_f32_e32 v26, v25
	v_sub_f32_e32 v25, v32, v28
	v_sub_f32_e32 v27, v33, v28
	v_exp_f32_e32 v112, v30
	v_sub_f32_e32 v30, v42, v28
	v_exp_f32_e32 v12, v12
	v_exp_f32_e32 v13, v13
	v_exp_f32_e32 v22, v22
	v_exp_f32_e32 v23, v23
	v_exp_f32_e32 v24, v24
	v_exp_f32_e32 v25, v25
	v_exp_f32_e32 v27, v27
	v_exp_f32_e32 v133, v30
	v_sub_f32_e32 v30, v43, v28
	v_exp_f32_e32 v134, v30
	v_sub_f32_e32 v30, v44, v28
	v_exp_f32_e32 v135, v30
	v_sub_f32_e32 v30, v45, v28
	v_sub_f32_e32 v29, v34, v28
	v_exp_f32_e32 v136, v30
	v_sub_f32_e32 v30, v76, v28
	v_exp_f32_e32 v29, v29
	v_exp_f32_e32 v137, v30
	v_sub_f32_e32 v30, v77, v28
	v_cvt_pk_f16_f32 v25, v25, v27
	v_cvt_pk_f16_f32 v24, v24, v26
	v_cvt_pk_f16_f32 v23, v22, v23
	v_cvt_pk_f16_f32 v22, v12, v13
	v_exp_f32_e32 v138, v30
	v_mov_b32_e32 v27, 0xc80
	v_mfma_f32_16x16x32_f16 v[30:33], v[116:119], v[22:25], 0
	ds_read_b64_tr_b16 v[12:13], v132 offset:16000
	ds_read_b64_tr_b16 v[34:35], v132 offset:12832
	v_cndmask_b32_e32 v27, 0, v27, vcc
	v_mfma_f32_16x16x32_f16 v[42:45], v[88:91], v[22:25], 0
	ds_read_b64_tr_b16 v[36:37], v132 offset:16032
	ds_read_b64_tr_b16 v[46:47], v132 offset:12864
	v_sub_f32_e32 v26, v78, v28
	v_mfma_f32_16x16x32_f16 v[84:87], v[120:123], v[22:25], 0
	ds_read_b64_tr_b16 v[48:49], v132 offset:16064
	ds_read_b64_tr_b16 v[88:89], v132 offset:12896
	v_add_u32_e32 v27, v132, v27
	v_mfma_f32_16x16x32_f16 v[92:95], v[92:95], v[22:25], 0
	ds_read_b64_tr_b16 v[90:91], v132 offset:16096
	ds_read_b64_tr_b16 v[108:109], v132 offset:12928
	v_exp_f32_e32 v26, v26
	v_mfma_f32_16x16x32_f16 v[22:25], v[96:99], v[22:25], 0
	v_cvt_pk_f16_f32 v99, v111, v112
	v_cvt_pk_f16_f32 v98, v53, v110
	ds_read_b64_tr_b16 v[110:111], v132 offset:16128
	v_cvt_pk_f16_f32 v97, v51, v52
	v_cvt_pk_f16_f32 v96, v29, v41
	v_sub_f32_e32 v29, v79, v28
	ds_read_b64_tr_b16 v[112:113], v132 offset:19200
	v_mfma_f32_16x16x32_f16 v[30:33], v[124:127], v[96:99], v[30:33]
	ds_read_b64_tr_b16 v[114:115], v27 offset:19200
	ds_read_b64_tr_b16 v[118:119], v27 offset:19232
	v_exp_f32_e32 v29, v29
	v_mfma_f32_16x16x32_f16 v[40:43], v[100:103], v[96:99], v[42:45]
	ds_read_b64_tr_b16 v[116:117], v132 offset:19232
	ds_read_b64_tr_b16 v[76:77], v132 offset:19264
	v_sub_f32_e32 v2, v2, v28
	v_mfma_f32_16x16x32_f16 v[80:83], v[80:83], v[96:99], v[84:87]
	ds_read_b64_tr_b16 v[78:79], v27 offset:19264
	v_cmp_gt_u32_e32 vcc, s4, v61
	s_nop 0
	ds_read_b64_tr_b16 v[84:85], v132 offset:19296
	v_mfma_f32_16x16x32_f16 v[92:95], v[128:131], v[96:99], v[92:95]
	ds_read_b64_tr_b16 v[86:87], v27 offset:19296
	ds_read_b64_tr_b16 v[100:101], v132 offset:19328
	v_mfma_f32_16x16x32_f16 v[22:25], v[104:107], v[96:99], v[22:25]
	ds_read_b64_tr_b16 v[102:103], v27 offset:19328
	ds_write_b64 v18, v[20:21] offset:57600
	v_mul_u32_u24_sdwa v18, v62, s7 dst_sel:DWORD dst_unused:UNUSED_PAD src0_sel:WORD_0 src1_sel:DWORD
	v_mul_i32_i24_sdwa v19, v18, s8 dst_sel:DWORD dst_unused:UNUSED_PAD src0_sel:WORD_1 src1_sel:DWORD
	v_mul_u32_u24_sdwa v14, v18, s6 dst_sel:DWORD dst_unused:UNUSED_PAD src0_sel:WORD_1 src1_sel:DWORD
	v_add_lshl_u32 v15, v19, v62, 3
	v_exp_f32_e32 v18, v2
	v_sub_f32_e32 v19, v3, v28
	v_sub_f32_e32 v2, v4, v28
	v_sub_f32_e32 v21, v5, v28
	v_cvt_pk_f16_f32 v99, v26, v29
	v_cvt_pk_f16_f32 v98, v137, v138
	v_cvt_pk_f16_f32 v97, v135, v136
	v_cvt_pk_f16_f32 v96, v133, v134
	v_add3_u32 v14, 0, v14, v15
	v_exp_f32_e32 v20, v2
	v_exp_f32_e32 v21, v21
	v_exp_f32_e32 v19, v19
	s_waitcnt lgkmcnt(14)
	v_mfma_f32_16x16x32_f16 v[10:13], v[10:13], v[96:99], v[30:33]
	ds_write_b64 v14, v[16:17] offset:57600
	v_mfma_f32_16x16x32_f16 v[14:17], v[34:37], v[96:99], v[40:43]
	v_mfma_f32_16x16x32_f16 v[30:33], v[46:49], v[96:99], v[80:83]
	s_nop 1
	v_mov_b32_e32 v42, 0
	v_cvt_pk_f16_f32 v41, v20, v21
	v_cvt_pk_f16_f32 v40, v18, v19
	s_waitcnt lgkmcnt(14)
	v_mfma_f32_16x16x32_f16 v[2:5], v[88:91], v[96:99], v[92:95]
	v_mov_b32_e32 v43, v42
	s_waitcnt lgkmcnt(12)
	v_mfma_f32_16x16x32_f16 v[34:37], v[108:111], v[96:99], v[22:25]
	s_waitcnt lgkmcnt(10)
	v_mfma_f32_16x16x32_f16 v[22:25], v[112:115], v[40:43], v[10:13]
	s_waitcnt lgkmcnt(8)
	v_mfma_f32_16x16x32_f16 v[18:21], v[116:119], v[40:43], v[14:17]
	s_waitcnt lgkmcnt(6)
	v_mfma_f32_16x16x32_f16 v[14:17], v[76:79], v[40:43], v[30:33]
	s_waitcnt lgkmcnt(4)
	v_mfma_f32_16x16x32_f16 v[10:13], v[84:87], v[40:43], v[2:5]
	s_waitcnt lgkmcnt(2)
	v_mfma_f32_16x16x32_f16 v[2:5], v[100:103], v[40:43], v[34:37]
	s_and_saveexec_b64 s[4:5], vcc
	s_cbranch_execz .LBB2_20
	v_mul_u32_u24_sdwa v26, v61, s7 dst_sel:DWORD dst_unused:UNUSED_PAD src0_sel:WORD_0 src1_sel:DWORD
	v_mul_i32_i24_sdwa v27, v26, s8 dst_sel:DWORD dst_unused:UNUSED_PAD src0_sel:WORD_1 src1_sel:DWORD
	s_waitcnt vmcnt(8)
	v_cvt_pk_f16_f32 v9, v8, v9
	v_cvt_pk_f16_f32 v8, v6, v7
	v_mul_u32_u24_sdwa v6, v26, s6 dst_sel:DWORD dst_unused:UNUSED_PAD src0_sel:WORD_1 src1_sel:DWORD
	v_add_lshl_u32 v7, v27, v61, 3
	v_add3_u32 v6, 0, v6, v7
	ds_write_b64 v6, v[8:9] offset:57600
